# v13 + dense-up SwiGLU epilogue split: second half (rows 128..255 of the tile) deferred into the next unit's first K-tile, 3/8 interleaved under its MFMAs
# speedup vs baseline: 1.0029x; 1.0029x over previous
.LBB0_1081:
	v_lshl_add_u64 v[10:11], s[22:23], 0, v[34:35]
	v_mov_b32_e32 v165, v35
	v_readlane_b32 s30, v253, 62
	v_bfe_u32 v189, v5, 4, 2
	s_lshl_b32 s5, s5, 5
	v_lshl_add_u64 v[12:13], s[22:23], 0, v[164:165]
	v_mov_b32_e32 v169, v35
	v_readlane_b32 s31, v253, 63
	v_and_b32_e32 v1, 15, v5
	v_lshlrev_b32_e32 v9, 4, v189
	v_lshlrev_b32_e32 v5, 2, v5
	s_and_b32 s46, s5, 0x60
	s_add_i32 m0, s41, 0x18000
	v_lshl_add_u64 v[10:11], v[10:11], 0, s[18:19]
	v_lshl_add_u64 v[14:15], s[30:31], 0, v[168:169]
	v_mov_b32_e32 v167, v35
	s_lshl_b32 s45, s8, 6
	v_lshl_or_b32 v9, v1, 6, v9
	s_lshl_b32 s8, s8, 13
	v_and_b32_e32 v5, 32, v5
	s_lshl_b32 s5, s46, 7
	s_waitcnt vmcnt(2)
	s_barrier
	global_load_lds_dwordx4 v[10:11], off
	v_lshl_add_u64 v[10:11], v[12:13], 0, s[18:19]
	s_add_i32 m0, s41, 0x1a000
	s_add_i32 s47, s41, 0x8000
	s_add_i32 s48, s41, 0xa000
	v_lshl_add_u64 v[16:17], s[30:31], 0, v[166:167]
	v_bitop3_b32 v18, v9, s8, v5 bitop3:0xde
	global_load_lds_dwordx4 v[10:11], off
	v_lshl_add_u64 v[10:11], v[14:15], 0, s[18:19]
	s_mov_b32 m0, s47
	s_add_u32 s8, s22, 0x20080
	global_load_lds_dwordx4 v[10:11], off
	v_lshl_add_u64 v[10:11], v[16:17], 0, s[18:19]
	s_mov_b32 m0, s48
	s_addc_u32 s9, s23, 0
	global_load_lds_dwordx4 v[10:11], off
	s_add_i32 m0, s41, 0x1c000
	v_lshl_add_u64 v[10:11], s[8:9], 0, v[34:35]
	global_load_lds_dwordx4 v[10:11], off
	v_lshl_add_u64 v[10:11], s[8:9], 0, v[164:165]
	s_add_i32 m0, s41, 0x1e000
	v_bitop3_b32 v196, v9, s5, v5 bitop3:0xde
	global_load_lds_dwordx4 v[10:11], off
	v_lshlrev_b32_e32 v5, 13, v7
	v_and_b32_e32 v5, 0xffffc000, v5
	v_lshl_add_u32 v5, v6, 10, v5
	v_and_b32_e32 v6, 1, v7
	v_lshl_or_b32 v5, v6, 6, v5
	v_lshl_add_u32 v170, v8, 1, v5
	v_lshlrev_b32_e32 v5, 13, v2
	v_and_b32_e32 v5, 0xffffc000, v5
	s_waitcnt vmcnt(6)
	v_lshl_add_u32 v3, v3, 10, v5
	v_and_b32_e32 v2, 1, v2
	s_cmpk_lt_u32 s4, 0x100
	v_lshl_or_b32 v2, v2, 6, v3
	v_mov_b32_e32 v36, 0
	s_cselect_b64 s[8:9], -1, 0
	v_mov_b32_e32 v171, v35
	v_lshl_add_u32 v172, v4, 1, v2
	v_mov_b32_e32 v173, v35
	s_mov_b32 s49, 0
	v_add_u32_e32 v197, 0, v18
	v_readlane_b32 s52, v253, 60
	v_readlane_b32 s53, v253, 59
	v_mov_b32_e32 v37, v36
	v_mov_b32_e32 v38, v36
	v_mov_b32_e32 v39, v36
	v_mov_b32_e32 v40, v36
	v_mov_b32_e32 v41, v36
	v_mov_b32_e32 v42, v36
	v_mov_b32_e32 v43, v36
	v_mov_b32_e32 v44, v36
	v_mov_b32_e32 v45, v36
	v_mov_b32_e32 v46, v36
	v_mov_b32_e32 v47, v36
	v_mov_b32_e32 v48, v36
	v_mov_b32_e32 v49, v36
	v_mov_b32_e32 v50, v36
	v_mov_b32_e32 v51, v36
	v_mov_b32_e32 v52, v36
	v_mov_b32_e32 v53, v36
	v_mov_b32_e32 v54, v36
	v_mov_b32_e32 v55, v36
	v_mov_b32_e32 v56, v36
	v_mov_b32_e32 v57, v36
	v_mov_b32_e32 v58, v36
	v_mov_b32_e32 v59, v36
	v_mov_b32_e32 v60, v36
	v_mov_b32_e32 v61, v36
	v_mov_b32_e32 v62, v36
	v_mov_b32_e32 v63, v36
	v_mov_b32_e32 v64, v36
	v_mov_b32_e32 v65, v36
	v_mov_b32_e32 v66, v36
	v_mov_b32_e32 v67, v36
	v_mov_b32_e32 v68, v36
	v_mov_b32_e32 v69, v36
	v_mov_b32_e32 v70, v36
	v_mov_b32_e32 v71, v36
	v_mov_b32_e32 v72, v36
	v_mov_b32_e32 v73, v36
	v_mov_b32_e32 v74, v36
	v_mov_b32_e32 v75, v36
	v_mov_b32_e32 v76, v36
	v_mov_b32_e32 v77, v36
	v_mov_b32_e32 v78, v36
	v_mov_b32_e32 v79, v36
	v_mov_b32_e32 v80, v36
	v_mov_b32_e32 v81, v36
	v_mov_b32_e32 v82, v36
	v_mov_b32_e32 v83, v36
	v_mov_b32_e32 v84, v36
	v_mov_b32_e32 v85, v36
	v_mov_b32_e32 v86, v36
	v_mov_b32_e32 v87, v36
	v_mov_b32_e32 v88, v36
	v_mov_b32_e32 v89, v36
	v_mov_b32_e32 v90, v36
	v_mov_b32_e32 v91, v36
	v_mov_b32_e32 v92, v36
	v_mov_b32_e32 v93, v36
	v_mov_b32_e32 v94, v36
	v_mov_b32_e32 v95, v36
	v_mov_b32_e32 v96, v36
	v_mov_b32_e32 v97, v36
	v_mov_b32_e32 v98, v36
	v_mov_b32_e32 v99, v36
	v_mov_b32_e32 v100, v36
	v_mov_b32_e32 v101, v36
	v_mov_b32_e32 v102, v36
	v_mov_b32_e32 v103, v36
	v_mov_b32_e32 v104, v36
	v_mov_b32_e32 v105, v36
	v_mov_b32_e32 v106, v36
	v_mov_b32_e32 v107, v36
	v_mov_b32_e32 v108, v36
	v_mov_b32_e32 v109, v36
	v_mov_b32_e32 v110, v36
	v_mov_b32_e32 v111, v36
	v_mov_b32_e32 v112, v36
	v_mov_b32_e32 v113, v36
	v_mov_b32_e32 v114, v36
	v_mov_b32_e32 v115, v36
	v_mov_b32_e32 v116, v36
	v_mov_b32_e32 v117, v36
	v_mov_b32_e32 v118, v36
	v_mov_b32_e32 v119, v36
	v_mov_b32_e32 v120, v36
	v_mov_b32_e32 v121, v36
	v_mov_b32_e32 v122, v36
	v_mov_b32_e32 v123, v36
	v_mov_b32_e32 v124, v36
	v_mov_b32_e32 v125, v36
	v_mov_b32_e32 v126, v36
	v_mov_b32_e32 v127, v36
	v_mov_b32_e32 v128, v36
	v_mov_b32_e32 v129, v36
	v_mov_b32_e32 v130, v36
	v_mov_b32_e32 v131, v36
	v_mov_b32_e32 v132, v36
	v_mov_b32_e32 v133, v36
	v_mov_b32_e32 v134, v36
	v_mov_b32_e32 v135, v36
	v_mov_b32_e32 v136, v36
	v_mov_b32_e32 v137, v36
	v_mov_b32_e32 v138, v36
	v_mov_b32_e32 v139, v36
	v_mov_b32_e32 v140, v36
	v_mov_b32_e32 v141, v36
	v_mov_b32_e32 v142, v36
	v_mov_b32_e32 v143, v36
	v_mov_b32_e32 v144, v36
	v_mov_b32_e32 v145, v36
	v_mov_b32_e32 v146, v36
	v_mov_b32_e32 v147, v36
	v_mov_b32_e32 v148, v36
	v_mov_b32_e32 v149, v36
	v_mov_b32_e32 v150, v36
	v_mov_b32_e32 v151, v36
	v_mov_b32_e32 v152, v36
	v_mov_b32_e32 v153, v36
	v_mov_b32_e32 v154, v36
	v_mov_b32_e32 v155, v36
	v_mov_b32_e32 v156, v36
	v_mov_b32_e32 v157, v36
	v_mov_b32_e32 v158, v36
	v_mov_b32_e32 v159, v36
	v_mov_b32_e32 v160, v36
	v_mov_b32_e32 v161, v36
	v_mov_b32_e32 v162, v36
	v_mov_b32_e32 v163, v36
	s_barrier
	s_mov_b32 s32, 0
	s_branch .LBB0_1084

.LBB0_1086:
	s_lshl_b32 s10, s51, 18
	s_add_u32 s10, s20, s10
	s_addc_u32 s11, s21, 0
	s_and_b64 s[16:17], s[4:5], exec
	s_cselect_b32 s54, s11, s31
	s_cselect_b32 s55, s10, s30
	s_lshl_b32 s14, s50, 18
	s_add_u32 s16, s15, s14
	s_addc_u32 s17, s26, 0
	s_and_b64 s[36:37], s[4:5], exec
	s_cselect_b32 s56, s17, s23
	s_cselect_b32 s57, s16, s22
	s_add_i32 s60, 0, 0x10000
	s_add_i32 s62, 0, 0x14000
	v_add_u32_e32 v198, s60, v196
	v_add_u32_e32 v199, s62, v196
	ds_read_b128 v[26:29], v198
	ds_read_b128 v[30:33], v198 offset:1024
	ds_read_b128 v[18:21], v198 offset:2048
	ds_read_b128 v[22:25], v198 offset:3072
	ds_read_b128 v[10:13], v199
	ds_read_b128 v[14:17], v199 offset:1024
	ds_read_b128 v[2:5], v199 offset:2048
	ds_read_b128 v[6:9], v199 offset:3072
	s_add_u32 s36, s30, 0x20080
	s_addc_u32 s37, s31, 0
	s_add_i32 s58, s41, 0xc000
	v_lshl_add_u64 v[174:175], s[36:37], 0, v[168:169]
	s_mov_b32 m0, s58
	s_add_i32 s59, s41, 0xe000
	ds_read_b128 v[200:203], v197
	ds_read_b128 v[204:207], v197 offset:1024
	ds_read_b128 v[222:225], v197 offset:2048
	ds_read_b128 v[226:229], v197 offset:3072
	ds_read_b128 v[230:233], v197 offset:4096
	ds_read_b128 v[234:237], v197 offset:5120
	ds_read_b128 v[238:241], v197 offset:6144
	ds_read_b128 v[242:245], v197 offset:7168
	global_load_lds_dwordx4 v[174:175], off
	v_lshl_add_u64 v[174:175], s[36:37], 0, v[166:167]
	s_mov_b32 m0, s59
	s_nop 0
	global_load_lds_dwordx4 v[174:175], off
	s_waitcnt vmcnt(8)
	s_waitcnt lgkmcnt(0)
	s_barrier
	s_setprio 1
	s_waitcnt lgkmcnt(0)
	s_mov_b32 vcc_lo, s32
	s_mov_b32 vcc_hi, 0
	s_cbranch_vccz .Lc1p_g3
	v_mfma_f32_16x16x128_f8f6f4 v[160:163], v[26:33], v[200:207], 0
	v_exp_f32_e64 v212, -v96
	v_exp_f32_e64 v213, -v97
	v_exp_f32_e64 v214, -v98
	v_exp_f32_e64 v215, -v99
	v_pk_mul_f32 v[216:217], v[96:97], v[64:65]
	v_mfma_f32_16x16x128_f8f6f4 v[156:159], v[18:25], v[200:207], 0
	v_pk_mul_f32 v[218:219], v[98:99], v[66:67]
	v_pk_add_f32 v[212:213], v[212:213], 1.0 op_sel_hi:[1,0]
	v_pk_add_f32 v[214:215], v[214:215], 1.0 op_sel_hi:[1,0]
	v_rcp_f32_e32 v212, v212
	v_rcp_f32_e32 v213, v213
	v_mfma_f32_16x16x128_f8f6f4 v[148:151], v[18:25], v[222:229], 0
	v_rcp_f32_e32 v214, v214
	v_rcp_f32_e32 v215, v215
	v_mov_b32_e32 v180, v35
	v_pk_mul_f32 v[216:217], v[212:213], v[216:217]
	v_pk_mul_f32 v[218:219], v[214:215], v[218:219]
	v_mfma_f32_16x16x128_f8f6f4 v[152:155], v[26:33], v[222:229], 0
	v_med3_f32 v216, v216, s13, v250
	v_med3_f32 v217, v217, s13, v250
	v_med3_f32 v218, v218, s13, v250
	v_med3_f32 v219, v219, s13, v250
	v_cvt_pk_fp8_f32 v180, v216, v217
	v_mfma_f32_16x16x128_f8f6f4 v[144:147], v[26:33], v[230:237], 0
	s_nop 0
	v_cvt_pk_fp8_f32 v180, v218, v219 op_sel:[0,0,1]
	v_exp_f32_e64 v212, -v92
	v_exp_f32_e64 v213, -v93
	v_exp_f32_e64 v214, -v94
	v_mfma_f32_16x16x128_f8f6f4 v[140:143], v[18:25], v[230:237], 0
	v_exp_f32_e64 v215, -v95
	v_pk_mul_f32 v[216:217], v[92:93], v[60:61]
	v_pk_mul_f32 v[218:219], v[94:95], v[62:63]
	v_pk_add_f32 v[212:213], v[212:213], 1.0 op_sel_hi:[1,0]
	v_pk_add_f32 v[214:215], v[214:215], 1.0 op_sel_hi:[1,0]
	v_mfma_f32_16x16x128_f8f6f4 v[132:135], v[18:25], v[238:245], 0
	v_rcp_f32_e32 v212, v212
	v_rcp_f32_e32 v213, v213
	v_rcp_f32_e32 v214, v214
	v_rcp_f32_e32 v215, v215
	v_mov_b32_e32 v181, v35
	v_mfma_f32_16x16x128_f8f6f4 v[136:139], v[26:33], v[238:245], 0
	v_pk_mul_f32 v[216:217], v[212:213], v[216:217]
	v_pk_mul_f32 v[218:219], v[214:215], v[218:219]
	v_med3_f32 v216, v216, s13, v250
	v_med3_f32 v217, v217, s13, v250
	v_med3_f32 v218, v218, s13, v250
	s_setprio 0
	s_setprio 1
	v_mfma_f32_16x16x128_f8f6f4 v[128:131], v[10:17], v[200:207], 0
	v_med3_f32 v219, v219, s13, v250
	v_cvt_pk_fp8_f32 v181, v216, v217
	s_nop 0
	v_cvt_pk_fp8_f32 v181, v218, v219 op_sel:[0,0,1]
	s_nop 0
	v_mfma_f32_16x16x128_f8f6f4 v[124:127], v[2:9], v[200:207], 0
	global_store_dwordx2 v[182:183], v[180:181], off
	v_add_co_u32_e32 v182, vcc, 0xb000, v182
	s_nop 1
	v_addc_co_u32_e32 v183, vcc, 0, v183, vcc
	v_exp_f32_e64 v212, -v88
	v_mfma_f32_16x16x128_f8f6f4 v[116:119], v[2:9], v[222:229], 0
	v_exp_f32_e64 v213, -v89
	v_exp_f32_e64 v214, -v90
	v_exp_f32_e64 v215, -v91
	v_pk_mul_f32 v[216:217], v[88:89], v[56:57]
	v_pk_mul_f32 v[218:219], v[90:91], v[58:59]
	v_mfma_f32_16x16x128_f8f6f4 v[120:123], v[10:17], v[222:229], 0
	v_pk_add_f32 v[212:213], v[212:213], 1.0 op_sel_hi:[1,0]
	v_pk_add_f32 v[214:215], v[214:215], 1.0 op_sel_hi:[1,0]
	v_rcp_f32_e32 v212, v212
	v_rcp_f32_e32 v213, v213
	v_rcp_f32_e32 v214, v214
	v_mfma_f32_16x16x128_f8f6f4 v[112:115], v[10:17], v[230:237], 0
	v_rcp_f32_e32 v215, v215
	v_mov_b32_e32 v180, v35
	v_pk_mul_f32 v[216:217], v[212:213], v[216:217]
	v_pk_mul_f32 v[218:219], v[214:215], v[218:219]
	v_med3_f32 v216, v216, s13, v250
	v_mfma_f32_16x16x128_f8f6f4 v[108:111], v[2:9], v[230:237], 0
	v_med3_f32 v217, v217, s13, v250
	v_med3_f32 v218, v218, s13, v250
	v_med3_f32 v219, v219, s13, v250
	v_cvt_pk_fp8_f32 v180, v216, v217
	s_nop 0
	v_mfma_f32_16x16x128_f8f6f4 v[100:103], v[2:9], v[238:245], 0
	v_cvt_pk_fp8_f32 v180, v218, v219 op_sel:[0,0,1]
	v_mfma_f32_16x16x128_f8f6f4 v[104:107], v[10:17], v[238:245], 0
	s_branch .Lc1d_g3
.Lc1p_g3:
	v_mfma_f32_16x16x128_f8f6f4 v[160:163], v[26:33], v[200:207], 0
	v_mfma_f32_16x16x128_f8f6f4 v[156:159], v[18:25], v[200:207], 0
	v_mfma_f32_16x16x128_f8f6f4 v[148:151], v[18:25], v[222:229], 0
	v_mfma_f32_16x16x128_f8f6f4 v[152:155], v[26:33], v[222:229], 0
	v_mfma_f32_16x16x128_f8f6f4 v[144:147], v[26:33], v[230:237], 0
	v_mfma_f32_16x16x128_f8f6f4 v[140:143], v[18:25], v[230:237], 0
	v_mfma_f32_16x16x128_f8f6f4 v[132:135], v[18:25], v[238:245], 0
	v_mfma_f32_16x16x128_f8f6f4 v[136:139], v[26:33], v[238:245], 0
	s_setprio 0
	s_setprio 1
	v_mfma_f32_16x16x128_f8f6f4 v[128:131], v[10:17], v[200:207], 0
	v_mfma_f32_16x16x128_f8f6f4 v[124:127], v[2:9], v[200:207], 0
	v_mfma_f32_16x16x128_f8f6f4 v[116:119], v[2:9], v[222:229], 0
	v_mfma_f32_16x16x128_f8f6f4 v[120:123], v[10:17], v[222:229], 0
	v_mfma_f32_16x16x128_f8f6f4 v[112:115], v[10:17], v[230:237], 0
	v_mfma_f32_16x16x128_f8f6f4 v[108:111], v[2:9], v[230:237], 0
	v_mfma_f32_16x16x128_f8f6f4 v[100:103], v[2:9], v[238:245], 0
	v_mfma_f32_16x16x128_f8f6f4 v[104:107], v[10:17], v[238:245], 0
.Lc1d_g3:
	s_setprio 0
	s_barrier
	s_add_i32 s60, s60, s40
	v_lshl_add_u64 v[174:175], s[22:23], 0, v[34:35]
	s_add_i32 s61, s60, 0x2000
	v_lshl_add_u64 v[178:179], v[174:175], 0, s[28:29]
	s_mov_b32 m0, s60
	v_lshl_add_u64 v[190:191], s[22:23], 0, v[164:165]
	s_add_u32 s36, s22, 0x20100
	ds_read_b128 v[200:203], v197 offset:16384
	ds_read_b128 v[204:207], v197 offset:17408
	ds_read_b128 v[222:225], v197 offset:18432
	ds_read_b128 v[226:229], v197 offset:19456
	ds_read_b128 v[230:233], v197 offset:20480
	ds_read_b128 v[234:237], v197 offset:21504
	ds_read_b128 v[238:241], v197 offset:22528
	ds_read_b128 v[242:245], v197 offset:23552
	s_mov_b32 vcc_lo, s32
	s_mov_b32 vcc_hi, 0
	s_cbranch_vccz .Le1skip_g3
	v_exp_f32_e64 v212, -v84
	v_exp_f32_e64 v213, -v85
	v_exp_f32_e64 v214, -v86
	v_exp_f32_e64 v215, -v87
	v_pk_mul_f32 v[216:217], v[84:85], v[52:53]
	v_pk_mul_f32 v[218:219], v[86:87], v[54:55]
	v_pk_add_f32 v[212:213], v[212:213], 1.0 op_sel_hi:[1,0]
	v_pk_add_f32 v[214:215], v[214:215], 1.0 op_sel_hi:[1,0]
	v_rcp_f32_e32 v212, v212
	v_rcp_f32_e32 v213, v213
	v_rcp_f32_e32 v214, v214
	v_rcp_f32_e32 v215, v215
	v_mov_b32_e32 v181, v35
	v_pk_mul_f32 v[216:217], v[212:213], v[216:217]
	v_pk_mul_f32 v[218:219], v[214:215], v[218:219]
	v_med3_f32 v216, v216, s13, v250
	v_med3_f32 v217, v217, s13, v250
	v_med3_f32 v218, v218, s13, v250
	v_med3_f32 v219, v219, s13, v250
	v_cvt_pk_fp8_f32 v181, v216, v217
	s_nop 0
	v_cvt_pk_fp8_f32 v181, v218, v219 op_sel:[0,0,1]
	s_nop 0
	global_store_dwordx2 v[182:183], v[180:181], off
	v_add_co_u32_e32 v182, vcc, 0xb000, v182
	s_nop 1
	v_addc_co_u32_e32 v183, vcc, 0, v183, vcc
	v_exp_f32_e64 v212, -v80
	v_exp_f32_e64 v213, -v81
	v_exp_f32_e64 v214, -v82
	v_exp_f32_e64 v215, -v83
	v_pk_mul_f32 v[216:217], v[80:81], v[48:49]
	v_pk_mul_f32 v[218:219], v[82:83], v[50:51]
	v_pk_add_f32 v[212:213], v[212:213], 1.0 op_sel_hi:[1,0]
	v_pk_add_f32 v[214:215], v[214:215], 1.0 op_sel_hi:[1,0]
	v_rcp_f32_e32 v212, v212
	v_rcp_f32_e32 v213, v213
	v_rcp_f32_e32 v214, v214
	v_rcp_f32_e32 v215, v215
	v_mov_b32_e32 v180, v35
	v_pk_mul_f32 v[216:217], v[212:213], v[216:217]
	v_pk_mul_f32 v[218:219], v[214:215], v[218:219]
	v_med3_f32 v216, v216, s13, v250
	v_med3_f32 v217, v217, s13, v250
	v_med3_f32 v218, v218, s13, v250
	v_med3_f32 v219, v219, s13, v250
	v_cvt_pk_fp8_f32 v180, v216, v217
	s_nop 0
	v_cvt_pk_fp8_f32 v180, v218, v219 op_sel:[0,0,1]
	v_exp_f32_e64 v212, -v76
	v_exp_f32_e64 v213, -v77
	v_exp_f32_e64 v214, -v78
	v_exp_f32_e64 v215, -v79
	v_pk_mul_f32 v[216:217], v[76:77], v[44:45]
	v_pk_mul_f32 v[218:219], v[78:79], v[46:47]
	v_pk_add_f32 v[212:213], v[212:213], 1.0 op_sel_hi:[1,0]
	v_pk_add_f32 v[214:215], v[214:215], 1.0 op_sel_hi:[1,0]
	v_rcp_f32_e32 v212, v212
	v_rcp_f32_e32 v213, v213
	v_rcp_f32_e32 v214, v214
	v_rcp_f32_e32 v215, v215
	v_mov_b32_e32 v181, v35
	v_pk_mul_f32 v[216:217], v[212:213], v[216:217]
	v_pk_mul_f32 v[218:219], v[214:215], v[218:219]
	v_med3_f32 v216, v216, s13, v250
	v_med3_f32 v217, v217, s13, v250
	v_med3_f32 v218, v218, s13, v250
	v_med3_f32 v219, v219, s13, v250
	v_cvt_pk_fp8_f32 v181, v216, v217
	s_nop 0
	v_cvt_pk_fp8_f32 v181, v218, v219 op_sel:[0,0,1]
	s_nop 0
	global_store_dwordx2 v[182:183], v[180:181], off
	v_add_co_u32_e32 v182, vcc, 0xb000, v182
	s_nop 1
	v_addc_co_u32_e32 v183, vcc, 0, v183, vcc
	v_exp_f32_e64 v212, -v72
	v_exp_f32_e64 v213, -v73
	v_exp_f32_e64 v214, -v74
	v_exp_f32_e64 v215, -v75
	v_pk_mul_f32 v[216:217], v[72:73], v[40:41]
	v_pk_mul_f32 v[218:219], v[74:75], v[42:43]
	v_pk_add_f32 v[212:213], v[212:213], 1.0 op_sel_hi:[1,0]
	v_pk_add_f32 v[214:215], v[214:215], 1.0 op_sel_hi:[1,0]
	v_rcp_f32_e32 v212, v212
	v_rcp_f32_e32 v213, v213
	v_rcp_f32_e32 v214, v214
	v_rcp_f32_e32 v215, v215
	v_mov_b32_e32 v180, v35
	v_pk_mul_f32 v[216:217], v[212:213], v[216:217]
	v_pk_mul_f32 v[218:219], v[214:215], v[218:219]
	v_med3_f32 v216, v216, s13, v250
	v_med3_f32 v217, v217, s13, v250
	v_med3_f32 v218, v218, s13, v250
	v_med3_f32 v219, v219, s13, v250
	v_cvt_pk_fp8_f32 v180, v216, v217
	s_nop 0
	v_cvt_pk_fp8_f32 v180, v218, v219 op_sel:[0,0,1]
	v_exp_f32_e64 v212, -v68
	v_exp_f32_e64 v213, -v69
	v_exp_f32_e64 v214, -v70
	v_exp_f32_e64 v215, -v71
	v_pk_mul_f32 v[216:217], v[68:69], v[36:37]
	v_pk_mul_f32 v[218:219], v[70:71], v[38:39]
	v_pk_add_f32 v[212:213], v[212:213], 1.0 op_sel_hi:[1,0]
	v_pk_add_f32 v[214:215], v[214:215], 1.0 op_sel_hi:[1,0]
	v_rcp_f32_e32 v212, v212
	v_rcp_f32_e32 v213, v213
	v_rcp_f32_e32 v214, v214
	v_rcp_f32_e32 v215, v215
	v_mov_b32_e32 v181, v35
	v_pk_mul_f32 v[216:217], v[212:213], v[216:217]
	v_pk_mul_f32 v[218:219], v[214:215], v[218:219]
	v_med3_f32 v216, v216, s13, v250
	v_med3_f32 v217, v217, s13, v250
	v_med3_f32 v218, v218, s13, v250
	v_med3_f32 v219, v219, s13, v250
	v_cvt_pk_fp8_f32 v181, v216, v217
	s_nop 0
	v_cvt_pk_fp8_f32 v181, v218, v219 op_sel:[0,0,1]
	s_nop 0
	global_store_dwordx2 v[182:183], v[180:181], off
.Le1skip_g3:
	global_load_lds_dwordx4 v[178:179], off
	v_lshl_add_u64 v[178:179], v[190:191], 0, s[28:29]
	s_mov_b32 m0, s61
	s_addc_u32 s37, s23, 0
	s_add_i32 s62, s62, s40
	global_load_lds_dwordx4 v[178:179], off
	v_lshl_add_u64 v[178:179], s[36:37], 0, v[34:35]
	s_mov_b32 m0, s62
	s_add_i32 s63, s62, 0x2000
	global_load_lds_dwordx4 v[178:179], off
	v_lshl_add_u64 v[178:179], s[36:37], 0, v[164:165]
	s_mov_b32 m0, s63
	v_lshl_add_u64 v[192:193], s[30:31], 0, v[168:169]
	global_load_lds_dwordx4 v[178:179], off
	v_lshl_add_u64 v[178:179], v[192:193], 0, s[28:29]
	s_mov_b32 m0, s41
	v_lshl_add_u64 v[194:195], s[30:31], 0, v[166:167]
	global_load_lds_dwordx4 v[178:179], off
	v_lshl_add_u64 v[178:179], v[194:195], 0, s[28:29]
	s_mov_b32 m0, s42
	s_nop 0
	global_load_lds_dwordx4 v[178:179], off
	s_mov_b32 vcc_lo, s32
	s_mov_b32 vcc_hi, 0
	s_cbranch_vccz .Lw8_g3
	s_waitcnt vmcnt(12)
	s_branch .Lwd_g3
.Lw8_g3:
	s_waitcnt vmcnt(8)
.Lwd_g3:
	s_waitcnt lgkmcnt(0)
	s_barrier
	s_setprio 1
	s_waitcnt lgkmcnt(0)
	v_mfma_f32_16x16x128_f8f6f4 v[96:99], v[26:33], v[200:207], 0
	v_mfma_f32_16x16x128_f8f6f4 v[92:95], v[18:25], v[200:207], 0
	v_mfma_f32_16x16x128_f8f6f4 v[84:87], v[18:25], v[222:229], 0
	v_mfma_f32_16x16x128_f8f6f4 v[88:91], v[26:33], v[222:229], 0
	v_mfma_f32_16x16x128_f8f6f4 v[80:83], v[26:33], v[230:237], 0
	v_mfma_f32_16x16x128_f8f6f4 v[76:79], v[18:25], v[230:237], 0
	v_mfma_f32_16x16x128_f8f6f4 v[68:71], v[18:25], v[238:245], 0
	v_mfma_f32_16x16x128_f8f6f4 v[72:75], v[26:33], v[238:245], 0
	s_setprio 0
	s_setprio 1
	v_mfma_f32_16x16x128_f8f6f4 v[64:67], v[10:17], v[200:207], 0
	v_mfma_f32_16x16x128_f8f6f4 v[60:63], v[2:9], v[200:207], 0
	v_mfma_f32_16x16x128_f8f6f4 v[52:55], v[2:9], v[222:229], 0
	v_mfma_f32_16x16x128_f8f6f4 v[56:59], v[10:17], v[222:229], 0
	v_mfma_f32_16x16x128_f8f6f4 v[48:51], v[10:17], v[230:237], 0
	v_mfma_f32_16x16x128_f8f6f4 v[44:47], v[2:9], v[230:237], 0
	v_mfma_f32_16x16x128_f8f6f4 v[36:39], v[2:9], v[238:245], 0
	v_mfma_f32_16x16x128_f8f6f4 v[40:43], v[10:17], v[238:245], 0
	s_setprio 0
	s_barrier
	s_add_i32 s64, 0, 0x18000
	s_add_i32 s66, 0, 0x1c000
	v_add_u32_e32 v200, s64, v196
	v_add_u32_e32 v201, s66, v196
	ds_read_b128 v[26:29], v200
	ds_read_b128 v[30:33], v200 offset:1024
	ds_read_b128 v[18:21], v200 offset:2048
	ds_read_b128 v[22:25], v200 offset:3072
	ds_read_b128 v[10:13], v201
	ds_read_b128 v[14:17], v201 offset:1024
	ds_read_b128 v[2:5], v201 offset:2048
	ds_read_b128 v[6:9], v201 offset:3072
	s_add_u32 s36, s30, 0x20100
	s_addc_u32 s37, s31, 0
	s_mov_b32 m0, s43
	v_lshl_add_u64 v[178:179], s[36:37], 0, v[168:169]
	ds_read_b128 v[202:205], v197 offset:32768
	ds_read_b128 v[206:209], v197 offset:33792
	ds_read_b128 v[222:225], v197 offset:34816
	ds_read_b128 v[226:229], v197 offset:35840
	ds_read_b128 v[230:233], v197 offset:36864
	ds_read_b128 v[234:237], v197 offset:37888
	ds_read_b128 v[238:241], v197 offset:38912
	ds_read_b128 v[242:245], v197 offset:39936
	global_load_lds_dwordx4 v[178:179], off
	v_lshl_add_u64 v[178:179], s[36:37], 0, v[166:167]
	s_mov_b32 m0, s44
	s_nop 0
	global_load_lds_dwordx4 v[178:179], off
	s_waitcnt vmcnt(8)
	s_waitcnt lgkmcnt(0)
	s_barrier
	s_setprio 1
	s_waitcnt lgkmcnt(0)
	v_mfma_f32_16x16x128_f8f6f4 v[160:163], v[26:33], v[202:209], v[160:163]
	v_mfma_f32_16x16x128_f8f6f4 v[156:159], v[18:25], v[202:209], v[156:159]
	v_mfma_f32_16x16x128_f8f6f4 v[148:151], v[18:25], v[222:229], v[148:151]
	v_mfma_f32_16x16x128_f8f6f4 v[152:155], v[26:33], v[222:229], v[152:155]
	v_mfma_f32_16x16x128_f8f6f4 v[144:147], v[26:33], v[230:237], v[144:147]
	v_mfma_f32_16x16x128_f8f6f4 v[140:143], v[18:25], v[230:237], v[140:143]
	v_mfma_f32_16x16x128_f8f6f4 v[132:135], v[18:25], v[238:245], v[132:135]
	v_mfma_f32_16x16x128_f8f6f4 v[136:139], v[26:33], v[238:245], v[136:139]
	s_setprio 0
	s_setprio 1
	v_mfma_f32_16x16x128_f8f6f4 v[128:131], v[10:17], v[202:209], v[128:131]
	v_mfma_f32_16x16x128_f8f6f4 v[124:127], v[2:9], v[202:209], v[124:127]
	v_mfma_f32_16x16x128_f8f6f4 v[116:119], v[2:9], v[222:229], v[116:119]
	v_mfma_f32_16x16x128_f8f6f4 v[120:123], v[10:17], v[222:229], v[120:123]
	v_mfma_f32_16x16x128_f8f6f4 v[112:115], v[10:17], v[230:237], v[112:115]
	v_mfma_f32_16x16x128_f8f6f4 v[108:111], v[2:9], v[230:237], v[108:111]
	v_mfma_f32_16x16x128_f8f6f4 v[100:103], v[2:9], v[238:245], v[100:103]
	v_mfma_f32_16x16x128_f8f6f4 v[104:107], v[10:17], v[238:245], v[104:107]
	s_setprio 0
	s_barrier
	s_add_i32 s64, s64, s40
	s_mov_b64 s[24:25], 0x180
	s_add_i32 s65, s64, 0x2000
	v_lshl_add_u64 v[174:175], v[174:175], 0, s[24:25]
	s_mov_b32 m0, s64
	s_add_u32 s36, s22, 0x20180
	ds_read_b128 v[202:205], v197 offset:49152
	ds_read_b128 v[206:209], v197 offset:50176
	ds_read_b128 v[222:225], v197 offset:51200
	ds_read_b128 v[226:229], v197 offset:52224
	ds_read_b128 v[230:233], v197 offset:53248
	ds_read_b128 v[234:237], v197 offset:54272
	ds_read_b128 v[238:241], v197 offset:55296
	ds_read_b128 v[242:245], v197 offset:56320
	global_load_lds_dwordx4 v[174:175], off
	v_lshl_add_u64 v[174:175], v[190:191], 0, s[24:25]
	s_mov_b32 m0, s65
	s_addc_u32 s37, s23, 0
	s_add_i32 s66, s66, s40
	global_load_lds_dwordx4 v[174:175], off
	v_lshl_add_u64 v[174:175], s[36:37], 0, v[34:35]
	s_mov_b32 m0, s66
	s_add_i32 s67, s66, 0x2000
	global_load_lds_dwordx4 v[174:175], off
	v_lshl_add_u64 v[174:175], s[36:37], 0, v[164:165]
	s_mov_b32 m0, s67
	s_nop 0
	global_load_lds_dwordx4 v[174:175], off
	v_lshl_add_u64 v[174:175], v[192:193], 0, s[24:25]
	s_mov_b32 m0, s47
	s_nop 0
	global_load_lds_dwordx4 v[174:175], off
	v_lshl_add_u64 v[174:175], v[194:195], 0, s[24:25]
	s_mov_b32 m0, s48
	s_nop 0
	global_load_lds_dwordx4 v[174:175], off
	s_waitcnt vmcnt(8)
	s_waitcnt lgkmcnt(0)
	s_barrier
	s_setprio 1
	s_waitcnt lgkmcnt(0)
	v_mfma_f32_16x16x128_f8f6f4 v[96:99], v[26:33], v[202:209], v[96:99]
	v_mfma_f32_16x16x128_f8f6f4 v[92:95], v[18:25], v[202:209], v[92:95]
	v_mfma_f32_16x16x128_f8f6f4 v[84:87], v[18:25], v[222:229], v[84:87]
	v_mfma_f32_16x16x128_f8f6f4 v[88:91], v[26:33], v[222:229], v[88:91]
	v_mfma_f32_16x16x128_f8f6f4 v[80:83], v[26:33], v[230:237], v[80:83]
	v_mfma_f32_16x16x128_f8f6f4 v[76:79], v[18:25], v[230:237], v[76:79]
	v_mfma_f32_16x16x128_f8f6f4 v[68:71], v[18:25], v[238:245], v[68:71]
	v_mfma_f32_16x16x128_f8f6f4 v[72:75], v[26:33], v[238:245], v[72:75]
	s_setprio 0
	s_setprio 1
	v_mfma_f32_16x16x128_f8f6f4 v[64:67], v[10:17], v[202:209], v[64:67]
	v_mfma_f32_16x16x128_f8f6f4 v[60:63], v[2:9], v[202:209], v[60:63]
	v_mfma_f32_16x16x128_f8f6f4 v[52:55], v[2:9], v[222:229], v[52:55]
	v_mfma_f32_16x16x128_f8f6f4 v[56:59], v[10:17], v[222:229], v[56:59]
	v_mfma_f32_16x16x128_f8f6f4 v[48:51], v[10:17], v[230:237], v[48:51]
	v_mfma_f32_16x16x128_f8f6f4 v[44:47], v[2:9], v[230:237], v[44:47]
	v_mfma_f32_16x16x128_f8f6f4 v[36:39], v[2:9], v[238:245], v[36:39]
	v_mfma_f32_16x16x128_f8f6f4 v[40:43], v[10:17], v[238:245], v[40:43]
	s_setprio 0
	s_barrier
	s_add_u32 s30, s30, 0x20180
	s_addc_u32 s31, s31, 0
	s_add_u32 s68, s22, 0x200
	s_addc_u32 s69, s23, 0
	s_mov_b32 s70, 0

.Lepi_nobar_2:
	v_pk_mul_f32 v[10:11], v[146:147], v[114:115]
	v_exp_f32_e64 v14, -v144
	v_exp_f32_e64 v15, -v145
	v_pk_mul_f32 v[10:11], v[18:19], v[10:11]
	v_exp_f32_e64 v18, -v142
	v_exp_f32_e64 v19, -v143
	v_pk_add_f32 v[14:15], v[14:15], 1.0 op_sel_hi:[1,0]
	v_pk_mul_f32 v[12:13], v[144:145], v[112:113]
	v_rcp_f32_e32 v14, v14
	v_rcp_f32_e32 v15, v15
	v_pk_add_f32 v[18:19], v[18:19], 1.0 op_sel_hi:[1,0]
	v_add_u32_e32 v7, 32, v6
	v_rcp_f32_e32 v18, v18
	v_rcp_f32_e32 v19, v19
	v_pk_mul_f32 v[12:13], v[14:15], v[12:13]
	v_pk_mul_f32 v[14:15], v[142:143], v[110:111]
	v_mad_i64_i32 v[8:9], s[22:23], v7, s14, v[4:5]
	v_pk_mul_f32 v[14:15], v[18:19], v[14:15]
	v_exp_f32_e64 v18, -v132
	v_exp_f32_e64 v19, -v133
	v_med3_f32 v7, v12, s13, v250
	v_med3_f32 v12, v13, s13, v250
	v_med3_f32 v13, v10, s13, v250
	v_mov_b32_e32 v10, v35
	v_cvt_pk_fp8_f32 v10, v7, v12
	v_pk_add_f32 v[18:19], v[18:19], 1.0 op_sel_hi:[1,0]
	v_med3_f32 v11, v11, s13, v250
	v_rcp_f32_e32 v18, v18
	v_rcp_f32_e32 v19, v19
	v_cvt_pk_fp8_f32 v10, v13, v11 op_sel:[0,0,1]
	v_med3_f32 v7, v16, s13, v250
	v_med3_f32 v12, v17, s13, v250
	v_mov_b32_e32 v11, v35
	v_pk_mul_f32 v[16:17], v[132:133], v[100:101]
	v_cvt_pk_fp8_f32 v11, v7, v12
	v_pk_mul_f32 v[16:17], v[18:19], v[16:17]
	v_exp_f32_e64 v18, -v138
	v_exp_f32_e64 v19, -v139
	v_med3_f32 v13, v14, s13, v250
	v_med3_f32 v14, v15, s13, v250
	v_cvt_pk_fp8_f32 v11, v13, v14 op_sel:[0,0,1]
	v_pk_add_f32 v[18:19], v[18:19], 1.0 op_sel_hi:[1,0]
	v_lshl_add_u64 v[8:9], v[8:9], 0, v[2:3]
	v_rcp_f32_e32 v18, v18
	v_rcp_f32_e32 v19, v19
	global_store_dwordx2 v[8:9], v[10:11], off
	v_pk_mul_f32 v[10:11], v[138:139], v[106:107]
	v_exp_f32_e64 v14, -v136
	v_exp_f32_e64 v15, -v137
	v_pk_mul_f32 v[10:11], v[18:19], v[10:11]
	v_exp_f32_e64 v18, -v134
	v_exp_f32_e64 v19, -v135
	v_pk_add_f32 v[14:15], v[14:15], 1.0 op_sel_hi:[1,0]
	v_pk_mul_f32 v[12:13], v[136:137], v[104:105]
	v_rcp_f32_e32 v14, v14
	v_rcp_f32_e32 v15, v15
	v_pk_add_f32 v[18:19], v[18:19], 1.0 op_sel_hi:[1,0]
	v_add_u32_e32 v7, 48, v6
	v_rcp_f32_e32 v18, v18
	v_rcp_f32_e32 v19, v19
	v_pk_mul_f32 v[12:13], v[14:15], v[12:13]
	v_pk_mul_f32 v[14:15], v[134:135], v[102:103]
	v_mad_i64_i32 v[8:9], s[22:23], v7, s14, v[4:5]
	v_pk_mul_f32 v[14:15], v[18:19], v[14:15]
	v_exp_f32_e64 v18, -v92
	v_exp_f32_e64 v19, -v93
	v_med3_f32 v7, v12, s13, v250
	v_med3_f32 v12, v13, s13, v250
	v_med3_f32 v13, v10, s13, v250
	v_mov_b32_e32 v10, v35
	v_cvt_pk_fp8_f32 v10, v7, v12
	v_pk_add_f32 v[18:19], v[18:19], 1.0 op_sel_hi:[1,0]
	v_med3_f32 v11, v11, s13, v250
	v_rcp_f32_e32 v18, v18
	v_rcp_f32_e32 v19, v19
	v_cvt_pk_fp8_f32 v10, v13, v11 op_sel:[0,0,1]
	v_med3_f32 v7, v16, s13, v250
	v_med3_f32 v12, v17, s13, v250
	v_mov_b32_e32 v11, v35
	v_pk_mul_f32 v[16:17], v[92:93], v[60:61]
	v_cvt_pk_fp8_f32 v11, v7, v12
	v_pk_mul_f32 v[16:17], v[18:19], v[16:17]
	v_exp_f32_e64 v18, -v98
	v_exp_f32_e64 v19, -v99
	v_med3_f32 v13, v14, s13, v250
	v_med3_f32 v14, v15, s13, v250
	v_cvt_pk_fp8_f32 v11, v13, v14 op_sel:[0,0,1]
	v_pk_add_f32 v[18:19], v[18:19], 1.0 op_sel_hi:[1,0]
	v_lshl_add_u64 v[8:9], v[8:9], 0, v[2:3]
	v_rcp_f32_e32 v18, v18
	v_rcp_f32_e32 v19, v19
	global_store_dwordx2 v[8:9], v[10:11], off
	v_add_u32_e32 v7, 0x80, v6
	v_mad_i64_i32 v[182:183], s[22:23], v7, s14, v[4:5]
	v_lshl_add_u64 v[182:183], v[182:183], 0, v[2:3]
	s_mov_b32 s32, 1
	s_mov_b64 s[22:23], -1
	s_andn2_b64 vcc, exec, s[4:5]
	s_mov_b32 s58, 0x19b00000
	v_readlane_b32 s59, v255, 10
	s_mov_b32 s60, 0xff61b1e6
	s_mov_b32 s56, 0x3a800000
	s_mov_b64 s[62:63], 0x800
	s_mov_b32 s64, 0x3b000000
	s_cbranch_vccnz .LBB0_1083
	s_andn2_b64 vcc, exec, s[6:7]
	s_cbranch_vccnz .LBB0_1082
	s_barrier
	s_branch .LBB0_1082
.LBB0_1093:
	v_exp_f32_e64 v212, -v96
	v_exp_f32_e64 v213, -v97
	v_exp_f32_e64 v214, -v98
	v_exp_f32_e64 v215, -v99
	v_pk_mul_f32 v[216:217], v[96:97], v[64:65]
	v_pk_mul_f32 v[218:219], v[98:99], v[66:67]
	v_pk_add_f32 v[212:213], v[212:213], 1.0 op_sel_hi:[1,0]
	v_pk_add_f32 v[214:215], v[214:215], 1.0 op_sel_hi:[1,0]
	v_rcp_f32_e32 v212, v212
	v_rcp_f32_e32 v213, v213
	v_rcp_f32_e32 v214, v214
	v_rcp_f32_e32 v215, v215
	v_mov_b32_e32 v180, v35
	v_pk_mul_f32 v[216:217], v[212:213], v[216:217]
	v_pk_mul_f32 v[218:219], v[214:215], v[218:219]
	v_med3_f32 v216, v216, s13, v250
	v_med3_f32 v217, v217, s13, v250
	v_med3_f32 v218, v218, s13, v250
	v_med3_f32 v219, v219, s13, v250
	v_cvt_pk_fp8_f32 v180, v216, v217
	s_nop 0
	v_cvt_pk_fp8_f32 v180, v218, v219 op_sel:[0,0,1]
	v_exp_f32_e64 v212, -v92
	v_exp_f32_e64 v213, -v93
	v_exp_f32_e64 v214, -v94
	v_exp_f32_e64 v215, -v95
	v_pk_mul_f32 v[216:217], v[92:93], v[60:61]
	v_pk_mul_f32 v[218:219], v[94:95], v[62:63]
	v_pk_add_f32 v[212:213], v[212:213], 1.0 op_sel_hi:[1,0]
	v_pk_add_f32 v[214:215], v[214:215], 1.0 op_sel_hi:[1,0]
	v_rcp_f32_e32 v212, v212
	v_rcp_f32_e32 v213, v213
	v_rcp_f32_e32 v214, v214
	v_rcp_f32_e32 v215, v215
	v_mov_b32_e32 v181, v35
	v_pk_mul_f32 v[216:217], v[212:213], v[216:217]
	v_pk_mul_f32 v[218:219], v[214:215], v[218:219]
	v_med3_f32 v216, v216, s13, v250
	v_med3_f32 v217, v217, s13, v250
	v_med3_f32 v218, v218, s13, v250
	v_med3_f32 v219, v219, s13, v250
	v_cvt_pk_fp8_f32 v181, v216, v217
	s_nop 0
	v_cvt_pk_fp8_f32 v181, v218, v219 op_sel:[0,0,1]
	s_nop 0
	global_store_dwordx2 v[182:183], v[180:181], off
	v_add_co_u32_e32 v182, vcc, 0xb000, v182
	s_nop 1
	v_addc_co_u32_e32 v183, vcc, 0, v183, vcc
	v_exp_f32_e64 v212, -v88
	v_exp_f32_e64 v213, -v89
	v_exp_f32_e64 v214, -v90
	v_exp_f32_e64 v215, -v91
	v_pk_mul_f32 v[216:217], v[88:89], v[56:57]
	v_pk_mul_f32 v[218:219], v[90:91], v[58:59]
	v_pk_add_f32 v[212:213], v[212:213], 1.0 op_sel_hi:[1,0]
	v_pk_add_f32 v[214:215], v[214:215], 1.0 op_sel_hi:[1,0]
	v_rcp_f32_e32 v212, v212
	v_rcp_f32_e32 v213, v213
	v_rcp_f32_e32 v214, v214
	v_rcp_f32_e32 v215, v215
	v_mov_b32_e32 v180, v35
	v_pk_mul_f32 v[216:217], v[212:213], v[216:217]
	v_pk_mul_f32 v[218:219], v[214:215], v[218:219]
	v_med3_f32 v216, v216, s13, v250
	v_med3_f32 v217, v217, s13, v250
	v_med3_f32 v218, v218, s13, v250
	v_med3_f32 v219, v219, s13, v250
	v_cvt_pk_fp8_f32 v180, v216, v217
	s_nop 0
	v_cvt_pk_fp8_f32 v180, v218, v219 op_sel:[0,0,1]
	v_exp_f32_e64 v212, -v84
	v_exp_f32_e64 v213, -v85
	v_exp_f32_e64 v214, -v86
	v_exp_f32_e64 v215, -v87
	v_pk_mul_f32 v[216:217], v[84:85], v[52:53]
	v_pk_mul_f32 v[218:219], v[86:87], v[54:55]
	v_pk_add_f32 v[212:213], v[212:213], 1.0 op_sel_hi:[1,0]
	v_pk_add_f32 v[214:215], v[214:215], 1.0 op_sel_hi:[1,0]
	v_rcp_f32_e32 v212, v212
	v_rcp_f32_e32 v213, v213
	v_rcp_f32_e32 v214, v214
	v_rcp_f32_e32 v215, v215
	v_mov_b32_e32 v181, v35
	v_pk_mul_f32 v[216:217], v[212:213], v[216:217]
	v_pk_mul_f32 v[218:219], v[214:215], v[218:219]
	v_med3_f32 v216, v216, s13, v250
	v_med3_f32 v217, v217, s13, v250
	v_med3_f32 v218, v218, s13, v250
	v_med3_f32 v219, v219, s13, v250
	v_cvt_pk_fp8_f32 v181, v216, v217
	s_nop 0
	v_cvt_pk_fp8_f32 v181, v218, v219 op_sel:[0,0,1]
	s_nop 0
	global_store_dwordx2 v[182:183], v[180:181], off
	v_add_co_u32_e32 v182, vcc, 0xb000, v182
	s_nop 1
	v_addc_co_u32_e32 v183, vcc, 0, v183, vcc
	v_exp_f32_e64 v212, -v80
	v_exp_f32_e64 v213, -v81
	v_exp_f32_e64 v214, -v82
	v_exp_f32_e64 v215, -v83
	v_pk_mul_f32 v[216:217], v[80:81], v[48:49]
	v_pk_mul_f32 v[218:219], v[82:83], v[50:51]
	v_pk_add_f32 v[212:213], v[212:213], 1.0 op_sel_hi:[1,0]
	v_pk_add_f32 v[214:215], v[214:215], 1.0 op_sel_hi:[1,0]
	v_rcp_f32_e32 v212, v212
	v_rcp_f32_e32 v213, v213
	v_rcp_f32_e32 v214, v214
	v_rcp_f32_e32 v215, v215
	v_mov_b32_e32 v180, v35
	v_pk_mul_f32 v[216:217], v[212:213], v[216:217]
	v_pk_mul_f32 v[218:219], v[214:215], v[218:219]
	v_med3_f32 v216, v216, s13, v250
	v_med3_f32 v217, v217, s13, v250
	v_med3_f32 v218, v218, s13, v250
	v_med3_f32 v219, v219, s13, v250
	v_cvt_pk_fp8_f32 v180, v216, v217
	s_nop 0
	v_cvt_pk_fp8_f32 v180, v218, v219 op_sel:[0,0,1]
	v_exp_f32_e64 v212, -v76
	v_exp_f32_e64 v213, -v77
	v_exp_f32_e64 v214, -v78
	v_exp_f32_e64 v215, -v79
	v_pk_mul_f32 v[216:217], v[76:77], v[44:45]
	v_pk_mul_f32 v[218:219], v[78:79], v[46:47]
	v_pk_add_f32 v[212:213], v[212:213], 1.0 op_sel_hi:[1,0]
	v_pk_add_f32 v[214:215], v[214:215], 1.0 op_sel_hi:[1,0]
	v_rcp_f32_e32 v212, v212
	v_rcp_f32_e32 v213, v213
	v_rcp_f32_e32 v214, v214
	v_rcp_f32_e32 v215, v215
	v_mov_b32_e32 v181, v35
	v_pk_mul_f32 v[216:217], v[212:213], v[216:217]
	v_pk_mul_f32 v[218:219], v[214:215], v[218:219]
	v_med3_f32 v216, v216, s13, v250
	v_med3_f32 v217, v217, s13, v250
	v_med3_f32 v218, v218, s13, v250
	v_med3_f32 v219, v219, s13, v250
	v_cvt_pk_fp8_f32 v181, v216, v217
	s_nop 0
	v_cvt_pk_fp8_f32 v181, v218, v219 op_sel:[0,0,1]
	s_nop 0
	global_store_dwordx2 v[182:183], v[180:181], off
	v_add_co_u32_e32 v182, vcc, 0xb000, v182
	s_nop 1
	v_addc_co_u32_e32 v183, vcc, 0, v183, vcc
	v_exp_f32_e64 v212, -v72
	v_exp_f32_e64 v213, -v73
	v_exp_f32_e64 v214, -v74
	v_exp_f32_e64 v215, -v75
	v_pk_mul_f32 v[216:217], v[72:73], v[40:41]
	v_pk_mul_f32 v[218:219], v[74:75], v[42:43]
	v_pk_add_f32 v[212:213], v[212:213], 1.0 op_sel_hi:[1,0]
	v_pk_add_f32 v[214:215], v[214:215], 1.0 op_sel_hi:[1,0]
	v_rcp_f32_e32 v212, v212
	v_rcp_f32_e32 v213, v213
	v_rcp_f32_e32 v214, v214
	v_rcp_f32_e32 v215, v215
	v_mov_b32_e32 v180, v35
	v_pk_mul_f32 v[216:217], v[212:213], v[216:217]
	v_pk_mul_f32 v[218:219], v[214:215], v[218:219]
	v_med3_f32 v216, v216, s13, v250
	v_med3_f32 v217, v217, s13, v250
	v_med3_f32 v218, v218, s13, v250
	v_med3_f32 v219, v219, s13, v250
	v_cvt_pk_fp8_f32 v180, v216, v217
	s_nop 0
	v_cvt_pk_fp8_f32 v180, v218, v219 op_sel:[0,0,1]
	v_exp_f32_e64 v212, -v68
	v_exp_f32_e64 v213, -v69
	v_exp_f32_e64 v214, -v70
	v_exp_f32_e64 v215, -v71
	v_pk_mul_f32 v[216:217], v[68:69], v[36:37]
	v_pk_mul_f32 v[218:219], v[70:71], v[38:39]
	v_pk_add_f32 v[212:213], v[212:213], 1.0 op_sel_hi:[1,0]
	v_pk_add_f32 v[214:215], v[214:215], 1.0 op_sel_hi:[1,0]
	v_rcp_f32_e32 v212, v212
	v_rcp_f32_e32 v213, v213
	v_rcp_f32_e32 v214, v214
	v_rcp_f32_e32 v215, v215
	v_mov_b32_e32 v181, v35
	v_pk_mul_f32 v[216:217], v[212:213], v[216:217]
	v_pk_mul_f32 v[218:219], v[214:215], v[218:219]
	v_med3_f32 v216, v216, s13, v250
	v_med3_f32 v217, v217, s13, v250
	v_med3_f32 v218, v218, s13, v250
	v_med3_f32 v219, v219, s13, v250
	v_cvt_pk_fp8_f32 v181, v216, v217
	s_nop 0
	v_cvt_pk_fp8_f32 v181, v218, v219 op_sel:[0,0,1]
	s_nop 0
	global_store_dwordx2 v[182:183], v[180:181], off
	s_waitcnt vmcnt(0)
	v_readlane_b32 s42, v254, 61
	v_readlane_b32 s44, v254, 63
	v_readlane_b32 s46, v255, 1
	v_readlane_b32 s43, v254, 62
	v_readlane_b32 s45, v255, 0
	v_readlane_b32 s47, v255, 2
	s_barrier
